# final-phase output stores marked nt, plus nt streaming loads and earlier edits
# speedup vs baseline: 1.0331x; 1.0042x over previous
.LBB0_2702:
	s_add_i32 s2, s2, s20
	v_lshl_add_u64 v[138:139], v[136:137], 0, s[10:11]
	s_cmpk_gt_i32 s2, 0x3fff
	v_lshl_add_u64 v[146:147], v[134:135], 0, s[4:5]
	v_lshl_add_u64 v[148:149], v[134:135], 0, s[6:7]
	v_lshl_add_u64 v[150:151], v[134:135], 0, s[8:9]
	v_lshl_add_u64 v[152:153], v[134:135], 0, s[10:11]
	v_lshl_add_u64 v[140:141], v[136:137], 0, s[4:5]
	v_lshl_add_u64 v[142:143], v[136:137], 0, s[6:7]
	v_lshl_add_u64 v[144:145], v[136:137], 0, s[8:9]
	global_store_dwordx4 v[134:135], v[12:15], off nt
	global_store_dwordx4 v[134:135], v[8:11], off offset:1024 nt
	global_store_dwordx4 v[134:135], v[4:7], off offset:2048 nt
	global_store_dwordx4 v[134:135], v[0:3], off offset:3072 nt
	global_store_dwordx4 v[146:147], v[28:31], off nt
	global_store_dwordx4 v[148:149], v[24:27], off nt
	global_store_dwordx4 v[150:151], v[20:23], off nt
	global_store_dwordx4 v[152:153], v[16:19], off nt
	global_store_dwordx4 v[136:137], v[36:39], off nt
	global_store_dwordx4 v[136:137], v[32:35], off offset:1024 nt
	global_store_dwordx4 v[136:137], v[40:43], off offset:2048 nt
	global_store_dwordx4 v[136:137], v[44:47], off offset:3072 nt
	global_store_dwordx4 v[140:141], v[52:55], off nt
	global_store_dwordx4 v[142:143], v[56:59], off nt
	global_store_dwordx4 v[144:145], v[60:63], off nt
	global_store_dwordx4 v[138:139], v[48:51], off nt
	s_cbranch_scc1 .LBB0_2726
